# baseline (speedup 1.0000x reference)
_Z7gemm1_kPKDF16_S0_PDF16_PKfPfS0_S1_:
	s_load_dwordx4 s[52:55], s[0:1], 0x28
	v_lshlrev_b32_e32 v52, 3, v0
	v_lshl_or_b32 v36, s2, 12, v52
	v_ashrrev_i32_e32 v37, 31, v36
	s_mov_b32 s3, 0x200000
	s_waitcnt lgkmcnt(0)
	v_lshl_add_u64 v[2:3], v[36:37], 1, s[52:53]
	v_add_co_u32_e32 v12, vcc, s3, v2
	s_mov_b32 s3, 0x400000
	s_nop 0
	v_addc_co_u32_e32 v13, vcc, 0, v3, vcc
	v_add_co_u32_e32 v20, vcc, s3, v2
	s_mov_b32 s3, 0x600000
	s_nop 0
	v_addc_co_u32_e32 v21, vcc, 0, v3, vcc
	v_add_co_u32_e32 v22, vcc, s3, v2
	global_load_dwordx4 v[4:7], v[2:3], off
	global_load_dwordx4 v[8:11], v[12:13], off
	v_addc_co_u32_e32 v23, vcc, 0, v3, vcc
	s_mov_b32 s3, 0x800000
	v_add_co_u32_e32 v28, vcc, s3, v2
	global_load_dwordx4 v[12:15], v[20:21], off
	global_load_dwordx4 v[16:19], v[22:23], off
	v_addc_co_u32_e32 v29, vcc, 0, v3, vcc
	s_mov_b32 s3, 0xa00000
	v_add_co_u32_e32 v30, vcc, s3, v2
	s_mov_b32 s3, 0xc00000
	s_nop 0
	v_addc_co_u32_e32 v31, vcc, 0, v3, vcc
	global_load_dwordx4 v[20:23], v[28:29], off
	global_load_dwordx4 v[24:27], v[30:31], off
	v_add_co_u32_e32 v28, vcc, s3, v2
	s_mov_b32 s3, 0xe00000
	s_nop 0
	v_addc_co_u32_e32 v29, vcc, 0, v3, vcc
	v_add_co_u32_e32 v2, vcc, s3, v2
	global_load_dwordx4 v[28:31], v[28:29], off
	s_nop 0
	v_addc_co_u32_e32 v3, vcc, 0, v3, vcc
	global_load_dwordx4 v[32:35], v[2:3], off
	v_ashrrev_i32_e32 v59, 10, v36
	s_mov_b32 s3, 0x3fffffe
	v_bfe_u32 v58, v0, 2, 1
	v_lshlrev_b32_e32 v2, 2, v0
	v_and_or_b32 v58, v59, s3, v58
	v_lshlrev_b32_e32 v59, 13, v0
	v_and_b32_e32 v53, 32, v2
	v_and_or_b32 v54, v52, 24, v53
	s_load_dwordx4 s[4:7], s[0:1], 0x0
	s_load_dwordx2 s[16:17], s[0:1], 0x18
	s_movk_i32 s12, 0xf80
	v_readfirstlane_b32 s3, v0
	s_lshl_b32 s3, s3, 4
	s_bfe_u32 s19, s2, 0x30003
	s_add_i32 s20, s3, 0
	s_waitcnt lgkmcnt(0)
	s_mov_b64 s[8:9], s[6:7]
	s_mov_b32 s7, 0x20000
	s_brev_b32 s6, -2
	s_add_i32 s21, s20, 0x10000
	s_and_b32 s9, s9, 0xffff
	s_mov_b32 m0, s21
	s_add_i32 s22, s20, 0x12000
	s_add_i32 s23, s20, 0x14000
	s_add_i32 s24, s20, 0x16000
	s_and_b32 s5, s5, 0xffff
	s_add_i32 s25, s20, 0x2000
	s_add_i32 s26, s20, 0x4000
	s_add_i32 s27, s20, 0x6000
	s_add_i32 s28, s20, 0x18000
	s_add_i32 s29, s20, 0x1a000
	s_add_i32 s30, s20, 0x1c000
	s_add_i32 s31, s20, 0x1e000
	s_add_i32 s33, s20, 0x8000
	s_add_i32 s34, s20, 0xa000
	v_cmp_lt_u32_e32 vcc, 63, v0
	v_lshrrev_b32_e32 v1, 3, v0
	v_lshlrev_b32_e32 v3, 4, v0
	v_xor_b32_e32 v1, v1, v0
	s_movk_i32 s11, 0x70
	s_movk_i32 s10, 0x1f80
	v_lshlrev_b32_e32 v60, 3, v1
	v_and_b32_e32 v61, 0x1f80, v3
	v_lshlrev_b32_e32 v62, 4, v1
	v_and_or_b32 v1, v62, s11, v61
	v_and_b32_e32 v61, 64, v62
	v_and_b32_e32 v60, 24, v60
	v_and_or_b32 v62, v52, s12, v53
	v_or3_b32 v60, v62, v61, v60
	v_lshlrev_b32_e32 v199, 1, v60
	v_or_b32_e32 v60, 0x2000, v3
	v_lshrrev_b32_e32 v61, 7, v60
	s_movk_i32 s12, 0x3f80
	v_mov_b32_e32 v63, 0x2000
	v_xor_b32_e32 v61, v61, v0
	v_bitop3_b32 v63, v3, s12, v63 bitop3:0xc8
	s_lshl_b32 s12, s2, 8
	v_lshlrev_b32_e32 v62, 3, v61
	v_lshlrev_b32_e32 v61, 4, v61
	v_lshrrev_b32_e32 v60, 1, v60
	s_and_b32 s18, s12, 0x700
	s_lshr_b32 s12, s2, 3
	s_lshl_b32 s2, s2, 2
	v_and_or_b32 v204, v61, s11, v63
	v_and_b32_e32 v61, 64, v61
	v_and_b32_e32 v62, 24, v62
	v_and_or_b32 v60, v60, s10, v53
	s_and_b32 s35, s2, 0xf00
	v_or3_b32 v60, v60, v61, v62
	s_mov_b32 s10, s6
	s_mov_b32 s11, s7
	s_add_i32 s18, s18, s12
	s_lshl_b32 s2, s35, 7
	v_lshlrev_b32_e32 v205, 1, v60
	s_lshr_b32 s12, s18, 4
	buffer_load_dwordx4 v199, s[8:11], s2 offen lds
	s_mov_b32 m0, s22
	s_and_b32 s12, s12, 0x3fffff8
	buffer_load_dwordx4 v205, s[8:11], s2 offen lds
	s_or_b32 s3, s2, 0x4000
	s_mov_b32 m0, s23
	s_or_b32 s12, s12, s19
	buffer_load_dwordx4 v199, s[8:11], s3 offen lds
	s_mov_b32 m0, s24
	s_nop 0
	buffer_load_dwordx4 v205, s[8:11], s3 offen lds
	s_lshl_b32 s3, s12, 15
	s_mov_b32 m0, s20
	s_or_b32 s13, s3, 0x4000
	buffer_load_dwordx4 v1, s[4:7], s3 offen lds
	s_mov_b32 m0, s25
	s_lshl_b32 s12, s12, 8
	buffer_load_dwordx4 v204, s[4:7], s3 offen lds
	s_mov_b32 m0, s26
	s_add_i32 s3, s3, 0x400000
	buffer_load_dwordx4 v1, s[4:7], s13 offen lds
	s_mov_b32 m0, s27
	s_nop 0
	buffer_load_dwordx4 v204, s[4:7], s13 offen lds
	s_or_b32 s13, s2, 0x80000
	s_mov_b32 m0, s28
	s_or_b32 s2, s2, 0x84000
	buffer_load_dwordx4 v199, s[8:11], s13 offen lds
	s_mov_b32 m0, s29
	s_nop 0
	buffer_load_dwordx4 v205, s[8:11], s13 offen lds
	s_mov_b32 m0, s30
	s_mov_b32 s13, 0
	buffer_load_dwordx4 v199, s[8:11], s2 offen lds
	s_mov_b32 m0, s31
	s_nop 0
	buffer_load_dwordx4 v205, s[8:11], s2 offen lds
	s_mov_b32 m0, s33
	s_nop 0
	buffer_load_dwordx4 v1, s[4:7], s3 offen lds
	s_mov_b32 m0, s34
	s_nop 0
	buffer_load_dwordx4 v204, s[4:7], s3 offen lds
	v_cmp_gt_u32_e64 s[2:3], 64, v0
	s_and_saveexec_b64 s[10:11], s[2:3]
	s_cbranch_execz .LBB3_2
	s_add_i32 s2, 0, 0x20000
	v_add_u32_e32 v3, s2, v3
	s_lshl_b64 s[2:3], s[12:13], 2
	s_add_u32 s2, s16, s2
	v_readfirstlane_b32 s13, v3
	s_addc_u32 s3, s17, s3
	v_lshlrev_b32_e32 v2, 2, v2
	s_mov_b32 m0, s13
	s_nop 0
	global_load_lds_dwordx4 v2, s[2:3]
	s_waitcnt vmcnt(0)
.LBB3_2:
	s_or_b64 exec, exec, s[10:11]
	s_waitcnt vmcnt(21)
	v_cvt_f32_f16_e32 v36, v4
	v_cvt_f32_f16_sdwa v37, v4 dst_sel:DWORD dst_unused:UNUSED_PAD src0_sel:WORD_1
	v_cvt_f32_f16_e32 v4, v5
	v_cvt_f32_f16_sdwa v5, v5 dst_sel:DWORD dst_unused:UNUSED_PAD src0_sel:WORD_1
	s_waitcnt vmcnt(20)
	v_cvt_f32_f16_e32 v38, v8
	v_cvt_f32_f16_sdwa v39, v8 dst_sel:DWORD dst_unused:UNUSED_PAD src0_sel:WORD_1
	s_waitcnt vmcnt(19)
	v_cvt_f32_f16_e32 v40, v12
	v_cvt_f32_f16_sdwa v41, v12 dst_sel:DWORD dst_unused:UNUSED_PAD src0_sel:WORD_1
	v_cvt_f32_f16_e32 v8, v9
	v_cvt_f32_f16_sdwa v9, v9 dst_sel:DWORD dst_unused:UNUSED_PAD src0_sel:WORD_1
	s_waitcnt vmcnt(18)
	v_cvt_f32_f16_e32 v42, v16
	v_cvt_f32_f16_sdwa v43, v16 dst_sel:DWORD dst_unused:UNUSED_PAD src0_sel:WORD_1
	v_cvt_f32_f16_e32 v12, v13
	v_cvt_f32_f16_sdwa v13, v13 dst_sel:DWORD dst_unused:UNUSED_PAD src0_sel:WORD_1
	v_cvt_f32_f16_e32 v16, v17
	s_waitcnt vmcnt(17)
	v_cvt_f32_f16_e32 v44, v20
	v_cvt_f32_f16_sdwa v45, v20 dst_sel:DWORD dst_unused:UNUSED_PAD src0_sel:WORD_1
	v_cvt_f32_f16_sdwa v17, v17 dst_sel:DWORD dst_unused:UNUSED_PAD src0_sel:WORD_1
	v_pk_add_f32 v[36:37], v[36:37], 0 op_sel_hi:[1,0]
	v_pk_add_f32 v[4:5], v[4:5], 0 op_sel_hi:[1,0]
	v_pk_add_f32 v[36:37], v[36:37], v[38:39]
	v_pk_add_f32 v[4:5], v[4:5], v[8:9]
	v_pk_add_f32 v[8:9], v[36:37], v[40:41]
	v_cvt_f32_f16_e32 v20, v21
	v_cvt_f32_f16_sdwa v21, v21 dst_sel:DWORD dst_unused:UNUSED_PAD src0_sel:WORD_1
	v_pk_add_f32 v[4:5], v[4:5], v[12:13]
	v_pk_add_f32 v[8:9], v[8:9], v[42:43]
	s_waitcnt vmcnt(16)
	v_cvt_f32_f16_e32 v46, v24
	v_cvt_f32_f16_sdwa v47, v24 dst_sel:DWORD dst_unused:UNUSED_PAD src0_sel:WORD_1
	v_pk_add_f32 v[12:13], v[4:5], v[16:17]
	v_pk_add_f32 v[4:5], v[8:9], v[44:45]
	v_cvt_f32_f16_e32 v8, v25
	v_cvt_f32_f16_sdwa v9, v25 dst_sel:DWORD dst_unused:UNUSED_PAD src0_sel:WORD_1
	s_waitcnt vmcnt(15)
	v_cvt_f32_f16_e32 v48, v28
	v_cvt_f32_f16_sdwa v49, v28 dst_sel:DWORD dst_unused:UNUSED_PAD src0_sel:WORD_1
	v_cvt_f32_f16_e32 v16, v29
	v_cvt_f32_f16_sdwa v17, v29 dst_sel:DWORD dst_unused:UNUSED_PAD src0_sel:WORD_1
	s_waitcnt vmcnt(14)
	v_cvt_f32_f16_e32 v50, v32
	v_cvt_f32_f16_sdwa v51, v32 dst_sel:DWORD dst_unused:UNUSED_PAD src0_sel:WORD_1
	v_cvt_f32_f16_e32 v24, v33
	v_cvt_f32_f16_sdwa v25, v33 dst_sel:DWORD dst_unused:UNUSED_PAD src0_sel:WORD_1
	v_pk_add_f32 v[12:13], v[12:13], v[20:21]
	v_pk_add_f32 v[4:5], v[4:5], v[46:47]
	v_pk_add_f32 v[8:9], v[12:13], v[8:9]
	v_pk_add_f32 v[4:5], v[4:5], v[48:49]
	v_pk_add_f32 v[8:9], v[8:9], v[16:17]
	v_pk_add_f32 v[4:5], v[4:5], v[50:51]
	v_pk_add_f32 v[8:9], v[8:9], v[24:25]
	v_cvt_pk_bf16_f32 v4, v4, v5
	v_cvt_pk_bf16_f32 v5, v8, v9
	v_cvt_f32_f16_e32 v8, v6
	v_cvt_f32_f16_sdwa v9, v6 dst_sel:DWORD dst_unused:UNUSED_PAD src0_sel:WORD_1
	v_cvt_f32_f16_e32 v12, v10
	v_cvt_f32_f16_sdwa v13, v10 dst_sel:DWORD dst_unused:UNUSED_PAD src0_sel:WORD_1
	v_cvt_f32_f16_e32 v16, v14
	v_cvt_f32_f16_sdwa v17, v14 dst_sel:DWORD dst_unused:UNUSED_PAD src0_sel:WORD_1
	v_cvt_f32_f16_e32 v20, v18
	v_cvt_f32_f16_sdwa v21, v18 dst_sel:DWORD dst_unused:UNUSED_PAD src0_sel:WORD_1
	v_pk_add_f32 v[8:9], v[8:9], 0 op_sel_hi:[1,0]
	v_cvt_f32_f16_e32 v24, v34
	v_pk_add_f32 v[8:9], v[8:9], v[12:13]
	v_cvt_f32_f16_e32 v12, v22
	v_cvt_f32_f16_sdwa v13, v22 dst_sel:DWORD dst_unused:UNUSED_PAD src0_sel:WORD_1
	v_pk_add_f32 v[8:9], v[8:9], v[16:17]
	v_cvt_f32_f16_e32 v16, v26
	v_cvt_f32_f16_sdwa v17, v26 dst_sel:DWORD dst_unused:UNUSED_PAD src0_sel:WORD_1
	v_pk_add_f32 v[8:9], v[8:9], v[20:21]
	v_cvt_f32_f16_e32 v20, v30
	v_cvt_f32_f16_sdwa v21, v30 dst_sel:DWORD dst_unused:UNUSED_PAD src0_sel:WORD_1
	v_cvt_f32_f16_sdwa v25, v34 dst_sel:DWORD dst_unused:UNUSED_PAD src0_sel:WORD_1
	v_pk_add_f32 v[8:9], v[8:9], v[12:13]
	v_cvt_f32_f16_e32 v10, v11
	v_pk_add_f32 v[8:9], v[8:9], v[16:17]
	v_cvt_f32_f16_sdwa v11, v11 dst_sel:DWORD dst_unused:UNUSED_PAD src0_sel:WORD_1
	v_pk_add_f32 v[8:9], v[8:9], v[20:21]
	v_cvt_f32_f16_e32 v12, v15
	v_pk_add_f32 v[8:9], v[8:9], v[24:25]
	v_cvt_f32_f16_sdwa v13, v15 dst_sel:DWORD dst_unused:UNUSED_PAD src0_sel:WORD_1
	v_cvt_pk_bf16_f32 v6, v8, v9
	v_cvt_f32_f16_e32 v8, v7
	v_cvt_f32_f16_sdwa v9, v7 dst_sel:DWORD dst_unused:UNUSED_PAD src0_sel:WORD_1
	v_cvt_f32_f16_e32 v14, v19
	v_cvt_f32_f16_sdwa v15, v19 dst_sel:DWORD dst_unused:UNUSED_PAD src0_sel:WORD_1
	v_cvt_f32_f16_e32 v16, v35
	v_pk_add_f32 v[8:9], v[8:9], 0 op_sel_hi:[1,0]
	v_cvt_f32_f16_sdwa v17, v35 dst_sel:DWORD dst_unused:UNUSED_PAD src0_sel:WORD_1
	v_pk_add_f32 v[8:9], v[8:9], v[10:11]
	v_cvt_f32_f16_e32 v10, v23
	v_cvt_f32_f16_sdwa v11, v23 dst_sel:DWORD dst_unused:UNUSED_PAD src0_sel:WORD_1
	v_pk_add_f32 v[8:9], v[8:9], v[12:13]
	v_cvt_f32_f16_e32 v12, v27
	v_cvt_f32_f16_sdwa v13, v27 dst_sel:DWORD dst_unused:UNUSED_PAD src0_sel:WORD_1
	v_pk_add_f32 v[8:9], v[8:9], v[14:15]
	v_cvt_f32_f16_e32 v14, v31
	v_cvt_f32_f16_sdwa v15, v31 dst_sel:DWORD dst_unused:UNUSED_PAD src0_sel:WORD_1
	v_pk_add_f32 v[8:9], v[8:9], v[10:11]
	s_nop 0
	v_pk_add_f32 v[8:9], v[8:9], v[12:13]
	v_lshlrev_b32_e32 v12, 6, v58
	v_pk_add_f32 v[8:9], v[8:9], v[14:15]
	v_ashrrev_i32_e32 v13, 31, v12
	v_pk_add_f32 v[8:9], v[8:9], v[16:17]
	v_cvt_pk_bf16_f32 v7, v8, v9
	v_and_b32_e32 v8, 0x1e0000, v59
	v_mov_b32_e32 v9, 0
	v_lshl_add_u64 v[10:11], s[54:55], 0, v[8:9]
	v_lshl_add_u64 v[10:11], v[12:13], 1, v[10:11]
	v_lshlrev_b32_e32 v8, 1, v54
	v_lshl_add_u64 v[8:9], v[10:11], 0, v[8:9]
	global_store_dwordx4 v[8:9], v[4:7], off
	s_load_dwordx2 s[10:11], s[0:1], 0x10
	v_lshrrev_b32_e32 v206, 8, v0
	v_lshrrev_b32_e32 v34, 2, v0
	v_cmp_eq_u32_e64 s[2:3], 1, v206
	s_and_saveexec_b64 s[14:15], s[2:3]
	s_cbranch_execz .LBB3_4
	s_barrier

	.amdhsa_kernel _Z7gemm1_kPKDF16_S0_PDF16_PKfPfS0_S1_
		.amdhsa_group_segment_fixed_size 0
		.amdhsa_private_segment_fixed_size 0
		.amdhsa_kernarg_size 56
		.amdhsa_user_sgpr_count 2
		.amdhsa_user_sgpr_dispatch_ptr 0
		.amdhsa_user_sgpr_queue_ptr 0
		.amdhsa_user_sgpr_kernarg_segment_ptr 1
		.amdhsa_user_sgpr_dispatch_id 0
		.amdhsa_user_sgpr_kernarg_preload_length 0
		.amdhsa_user_sgpr_kernarg_preload_offset 0
		.amdhsa_user_sgpr_private_segment_size 0
		.amdhsa_uses_dynamic_stack 0
		.amdhsa_enable_private_segment 0
		.amdhsa_system_sgpr_workgroup_id_x 1
		.amdhsa_system_sgpr_workgroup_id_y 0
		.amdhsa_system_sgpr_workgroup_id_z 0
		.amdhsa_system_sgpr_workgroup_info 0
		.amdhsa_system_vgpr_workitem_id 0
		.amdhsa_next_free_vgpr 228
		.amdhsa_next_free_sgpr 56
		.amdhsa_accum_offset 228
		.amdhsa_reserve_vcc 1
		.amdhsa_float_round_mode_32 0
		.amdhsa_float_round_mode_16_64 0
		.amdhsa_float_denorm_mode_32 3
		.amdhsa_float_denorm_mode_16_64 3
		.amdhsa_dx10_clamp 1
		.amdhsa_ieee_mode 1
		.amdhsa_fp16_overflow 0
		.amdhsa_tg_split 0
		.amdhsa_exception_fp_ieee_invalid_op 0
		.amdhsa_exception_fp_denorm_src 0
		.amdhsa_exception_fp_ieee_div_zero 0
		.amdhsa_exception_fp_ieee_overflow 0
		.amdhsa_exception_fp_ieee_underflow 0
		.amdhsa_exception_fp_ieee_inexact 0
		.amdhsa_exception_int_div_zero 0
	.end_amdhsa_kernel

_Z6gemm_kILi2EEvPKDF16_S1_iiiiPfPDF16_PKfS2_:
	s_lshl_b32 s3, s2, 3
	s_load_dwordx2 s[46:47], s[0:1], 0x30
	s_load_dwordx2 s[4:5], s[0:1], 0x8
	s_load_dwordx2 s[8:9], s[0:1], 0x0
	s_load_dwordx2 s[14:15], s[0:1], 0x28
	s_and_b32 s18, s3, 56
	s_ashr_i32 s3, s2, 5
	s_add_i32 s18, s18, s3
	s_lshl_b32 s6, s18, 8
	s_and_b32 s13, s6, 0xf00
	s_ashr_i32 s12, s18, 4
	v_lshrrev_b32_e32 v132, 8, v0
	v_readfirstlane_b32 s3, v0
	s_mul_i32 s16, s12, 0x84
	s_ashr_i32 s17, s16, 31
	s_lshl_b64 s[48:49], s[16:17], 19
	s_add_i32 s20, 0, 0x20000
	s_mov_b32 s7, 0x20000
	s_brev_b32 s6, -2
	s_movk_i32 s50, 0x100
	s_waitcnt lgkmcnt(0)
	v_cmp_gt_u32_e64 s[0:1], s50, v0
	s_add_u32 s4, s4, s48
	s_addc_u32 s48, s5, s49
	s_and_b32 s5, s48, 0xffff
	s_lshl_b32 s50, s13, 2
	s_add_u32 s46, s46, s50
	s_addc_u32 s47, s47, 0
	v_lshrrev_b32_e32 v1, 3, v0
	v_lshlrev_b32_e32 v2, 4, v0
	v_xor_b32_e32 v1, v1, v0
	v_and_b32_e32 v4, 0x1f80, v2
	v_lshlrev_b32_e32 v5, 4, v1
	s_movk_i32 s18, 0x70
	v_lshlrev_b32_e32 v6, 2, v0
	v_lshlrev_b32_e32 v3, 3, v1
	v_and_or_b32 v1, v5, s18, v4
	v_lshlrev_b32_e32 v4, 3, v0
	v_and_b32_e32 v6, 32, v6
	s_movk_i32 s19, 0xf80
	v_and_b32_e32 v5, 64, v5
	v_and_b32_e32 v3, 24, v3
	v_and_or_b32 v4, v4, s19, v6
	v_or3_b32 v3, v4, v5, v3
	v_lshlrev_b32_e32 v130, 1, v3
	v_or_b32_e32 v3, 0x2000, v2
	s_lshl_b32 s10, s2, 5
	v_lshrrev_b32_e32 v4, 7, v3
	s_and_b32 s21, s10, 0x300
	s_lshl_b32 s3, s3, 4
	s_lshl_b64 s[10:11], s[16:17], 17
	v_xor_b32_e32 v4, v4, v0
	s_movk_i32 s19, 0x3f80
	v_mov_b32_e32 v7, 0x2000
	s_add_u32 s8, s8, s10
	v_lshlrev_b32_e32 v5, 3, v4
	v_bitop3_b32 v2, v2, s19, v7 bitop3:0xc8
	v_lshlrev_b32_e32 v4, 4, v4
	s_addc_u32 s9, s9, s11
	s_movk_i32 s17, 0x1f80
	v_and_or_b32 v131, v4, s18, v2
	v_lshrrev_b32_e32 v2, 1, v3
	s_add_i32 s3, s3, 0
	v_and_b32_e32 v3, 64, v4
	v_and_b32_e32 v4, 24, v5
	v_and_or_b32 v2, v2, s17, v6
	s_add_i32 s17, s3, 0x10000
	v_or3_b32 v2, v2, v3, v4
	s_lshl_b32 s18, s13, 7
	s_mov_b32 m0, s17
	s_add_i32 s22, s3, 0x12000
	s_lshl_b32 s23, s13, 6
	v_lshlrev_b32_e32 v133, 1, v2
	buffer_load_dwordx4 v130, s[4:7], s18 offen lds
	s_mov_b32 m0, s22
	s_or_b32 s24, s23, 0x2000
	s_add_i32 s25, s3, 0x14000
	buffer_load_dwordx4 v133, s[4:7], s18 offen lds
	s_lshl_b32 s19, s24, 1
	s_mov_b32 m0, s25
	s_add_i32 s26, s3, 0x16000
	buffer_load_dwordx4 v130, s[4:7], s19 offen lds
	s_mov_b32 m0, s26
	s_and_b32 s9, s9, 0xffff
	s_mov_b32 s11, 0x20000
	s_brev_b32 s10, -2
	buffer_load_dwordx4 v133, s[4:7], s19 offen lds
	s_lshl_b32 s28, s21, 7
	s_mov_b32 m0, s3
	s_add_i32 s27, s3, 0x2000
	buffer_load_dwordx4 v1, s[8:11], s28 offen lds
	s_mov_b32 m0, s27
	s_add_i32 s30, s3, 0x4000
	buffer_load_dwordx4 v131, s[8:11], s28 offen lds
	s_lshl_b32 s28, s21, 6
	s_or_b32 s29, s28, 0x2000
	s_lshl_b32 s33, s29, 1
	s_mov_b32 m0, s30
	s_add_i32 s31, s3, 0x6000
	buffer_load_dwordx4 v1, s[8:11], s33 offen lds
	s_mov_b32 m0, s31
	s_bitset1_b32 s18, 19
	buffer_load_dwordx4 v131, s[8:11], s33 offen lds
	s_add_i32 s33, s3, 0x18000
	s_mov_b32 m0, s33
	s_add_i32 s34, s3, 0x1a000
	buffer_load_dwordx4 v130, s[4:7], s18 offen lds
	s_mov_b32 m0, s34
	s_add_i32 s35, s3, 0x1c000
	buffer_load_dwordx4 v133, s[4:7], s18 offen lds
	s_bitset1_b32 s19, 19
	s_mov_b32 m0, s35
	s_add_i32 s36, s3, 0x1e000
	buffer_load_dwordx4 v130, s[4:7], s19 offen lds
	s_mov_b32 m0, s36
	s_mov_b32 s37, 2
	buffer_load_dwordx4 v133, s[4:7], s19 offen lds
	v_and_b32_e32 v221, 0xff, v0
	v_lshlrev_b32_e32 v220, 2, v221
	s_lshr_b32 s50, s3, 12
	s_lshl_b32 s50, s50, 4
	s_lshl_b32 s51, s12, 6
	s_add_i32 s50, s50, s51
	s_lshl_b32 s50, s50, 14
	s_add_u32 s46, s46, s50
	s_addc_u32 s47, s47, 0
	global_load_dword v10, v220, s[46:47]
	s_add_u32 s46, s46, 0x4000
	s_addc_u32 s47, s47, 0
	global_load_dword v11, v220, s[46:47]
	s_add_u32 s46, s46, 0x4000
	s_addc_u32 s47, s47, 0
	global_load_dword v12, v220, s[46:47]
	s_add_u32 s46, s46, 0x4000
	s_addc_u32 s47, s47, 0
	global_load_dword v13, v220, s[46:47]
	s_add_u32 s46, s46, 0x4000
	s_addc_u32 s47, s47, 0
	global_load_dword v14, v220, s[46:47]
	s_add_u32 s46, s46, 0x4000
	s_addc_u32 s47, s47, 0
	global_load_dword v15, v220, s[46:47]
	s_add_u32 s46, s46, 0x4000
	s_addc_u32 s47, s47, 0
	global_load_dword v16, v220, s[46:47]
	s_add_u32 s46, s46, 0x4000
	s_addc_u32 s47, s47, 0
	global_load_dword v17, v220, s[46:47]
	s_add_u32 s46, s46, 0x4000
	s_addc_u32 s47, s47, 0
	global_load_dword v18, v220, s[46:47]
	s_add_u32 s46, s46, 0x4000
	s_addc_u32 s47, s47, 0
	global_load_dword v19, v220, s[46:47]
	s_add_u32 s46, s46, 0x4000
	s_addc_u32 s47, s47, 0
	global_load_dword v20, v220, s[46:47]
	s_add_u32 s46, s46, 0x4000
	s_addc_u32 s47, s47, 0
	global_load_dword v21, v220, s[46:47]
	s_add_u32 s46, s46, 0x4000
	s_addc_u32 s47, s47, 0
	global_load_dword v22, v220, s[46:47]
	s_add_u32 s46, s46, 0x4000
	s_addc_u32 s47, s47, 0
	global_load_dword v23, v220, s[46:47]
	s_add_u32 s46, s46, 0x4000
	s_addc_u32 s47, s47, 0
	global_load_dword v24, v220, s[46:47]
	s_add_u32 s46, s46, 0x4000
	s_addc_u32 s47, s47, 0
	global_load_dword v25, v220, s[46:47]
	s_add_u32 s46, s46, 0x44000
	s_addc_u32 s47, s47, 0
	global_load_dword v26, v220, s[46:47]
	s_add_u32 s46, s46, 0x4000
	s_addc_u32 s47, s47, 0
	global_load_dword v27, v220, s[46:47]
	s_add_u32 s46, s46, 0x4000
	s_addc_u32 s47, s47, 0
	global_load_dword v28, v220, s[46:47]
	s_add_u32 s46, s46, 0x4000
	s_addc_u32 s47, s47, 0
	global_load_dword v29, v220, s[46:47]
	s_add_u32 s46, s46, 0x4000
	s_addc_u32 s47, s47, 0
	global_load_dword v30, v220, s[46:47]
	s_add_u32 s46, s46, 0x4000
	s_addc_u32 s47, s47, 0
	global_load_dword v31, v220, s[46:47]
	s_add_u32 s46, s46, 0x4000
	s_addc_u32 s47, s47, 0
	global_load_dword v32, v220, s[46:47]
	s_add_u32 s46, s46, 0x4000
	s_addc_u32 s47, s47, 0
	global_load_dword v33, v220, s[46:47]
	s_add_u32 s46, s46, 0x4000
	s_addc_u32 s47, s47, 0
	global_load_dword v34, v220, s[46:47]
	s_add_u32 s46, s46, 0x4000
	s_addc_u32 s47, s47, 0
	global_load_dword v35, v220, s[46:47]
	s_add_u32 s46, s46, 0x4000
	s_addc_u32 s47, s47, 0
	global_load_dword v36, v220, s[46:47]
	s_add_u32 s46, s46, 0x4000
	s_addc_u32 s47, s47, 0
	global_load_dword v37, v220, s[46:47]
	s_add_u32 s46, s46, 0x4000
	s_addc_u32 s47, s47, 0
	global_load_dword v38, v220, s[46:47]
	s_add_u32 s46, s46, 0x4000
	s_addc_u32 s47, s47, 0
	global_load_dword v39, v220, s[46:47]
	s_add_u32 s46, s46, 0x4000
	s_addc_u32 s47, s47, 0
	global_load_dword v40, v220, s[46:47]
	s_add_u32 s46, s46, 0x4000
	s_addc_u32 s47, s47, 0
	global_load_dword v41, v220, s[46:47]
	v_mov_b32_e32 v8, 0
	s_cmp_lt_i32 s12, 1
	s_cbranch_scc1 .Lg2_skip0
	s_sub_u32 s46, s46, 0x13c000
	s_subb_u32 s47, s47, 0
	global_load_dword v42, v220, s[46:47]
	s_add_u32 s46, s46, 0x4000
	s_addc_u32 s47, s47, 0
	global_load_dword v43, v220, s[46:47]
	s_add_u32 s46, s46, 0x4000
	s_addc_u32 s47, s47, 0
	global_load_dword v44, v220, s[46:47]
	s_add_u32 s46, s46, 0x4000
	s_addc_u32 s47, s47, 0
	global_load_dword v45, v220, s[46:47]
	s_add_u32 s46, s46, 0x4000
	s_addc_u32 s47, s47, 0
	global_load_dword v46, v220, s[46:47]
	s_add_u32 s46, s46, 0x4000
	s_addc_u32 s47, s47, 0
	global_load_dword v47, v220, s[46:47]
	s_add_u32 s46, s46, 0x4000
	s_addc_u32 s47, s47, 0
	global_load_dword v48, v220, s[46:47]
	s_add_u32 s46, s46, 0x4000
	s_addc_u32 s47, s47, 0
	global_load_dword v49, v220, s[46:47]
	s_add_u32 s46, s46, 0x4000
	s_addc_u32 s47, s47, 0
	global_load_dword v50, v220, s[46:47]
	s_add_u32 s46, s46, 0x4000
	s_addc_u32 s47, s47, 0
	global_load_dword v51, v220, s[46:47]
	s_add_u32 s46, s46, 0x4000
	s_addc_u32 s47, s47, 0
	global_load_dword v52, v220, s[46:47]
	s_add_u32 s46, s46, 0x4000
	s_addc_u32 s47, s47, 0
	global_load_dword v53, v220, s[46:47]
	s_add_u32 s46, s46, 0x4000
	s_addc_u32 s47, s47, 0
	global_load_dword v54, v220, s[46:47]
	s_add_u32 s46, s46, 0x4000
	s_addc_u32 s47, s47, 0
	global_load_dword v55, v220, s[46:47]
	s_add_u32 s46, s46, 0x4000
	s_addc_u32 s47, s47, 0
	global_load_dword v56, v220, s[46:47]
	s_add_u32 s46, s46, 0x4000
	s_addc_u32 s47, s47, 0
	global_load_dword v57, v220, s[46:47]
.Lg2_skip0:
	s_waitcnt vmcnt(0)
	v_add_f32_e32 v3, 0, v10
	v_add_f32_e32 v3, v3, v11
	v_add_f32_e32 v3, v3, v12
	v_add_f32_e32 v3, v3, v13
	v_add_f32_e32 v3, v3, v14
	v_add_f32_e32 v3, v3, v15
	v_add_f32_e32 v3, v3, v16
	v_add_f32_e32 v3, v3, v17
	v_add_f32_e32 v3, v3, v18
	v_add_f32_e32 v3, v3, v19
	v_add_f32_e32 v3, v3, v20
	v_add_f32_e32 v3, v3, v21
	v_add_f32_e32 v3, v3, v22
	v_add_f32_e32 v3, v3, v23
	v_add_f32_e32 v3, v3, v24
	v_add_f32_e32 v3, v3, v25
	v_add_f32_e32 v4, 0, v26
	v_add_f32_e32 v4, v4, v27
	v_add_f32_e32 v4, v4, v28
	v_add_f32_e32 v4, v4, v29
	v_add_f32_e32 v4, v4, v30
	v_add_f32_e32 v4, v4, v31
	v_add_f32_e32 v4, v4, v32
	v_add_f32_e32 v4, v4, v33
	v_add_f32_e32 v4, v4, v34
	v_add_f32_e32 v4, v4, v35
	v_add_f32_e32 v4, v4, v36
	v_add_f32_e32 v4, v4, v37
	v_add_f32_e32 v4, v4, v38
	v_add_f32_e32 v4, v4, v39
	v_add_f32_e32 v4, v4, v40
	v_add_f32_e32 v4, v4, v41
	s_cmp_lt_i32 s12, 1
	s_cbranch_scc1 .Lg2_skip0b
	v_add_f32_e32 v8, 0, v42
	v_add_f32_e32 v8, v8, v43
	v_add_f32_e32 v8, v8, v44
	v_add_f32_e32 v8, v8, v45
	v_add_f32_e32 v8, v8, v46
	v_add_f32_e32 v8, v8, v47
	v_add_f32_e32 v8, v8, v48
	v_add_f32_e32 v8, v8, v49
	v_add_f32_e32 v8, v8, v50
	v_add_f32_e32 v8, v8, v51
	v_add_f32_e32 v8, v8, v52
	v_add_f32_e32 v8, v8, v53
	v_add_f32_e32 v8, v8, v54
	v_add_f32_e32 v8, v8, v55
	v_add_f32_e32 v8, v8, v56
	v_add_f32_e32 v8, v8, v57
.Lg2_skip0b:
	v_mul_u32_u24_e32 v5, 0xc00, v132
	v_add3_u32 v2, s20, v5, v220
	ds_write2st64_b32 v2, v8, v3 offset0:12 offset1:16
	ds_write_b32 v2, v4 offset:5120
	s_waitcnt lgkmcnt(0)
	s_barrier
	s_and_saveexec_b64 s[50:51], s[0:1]
	s_cbranch_execz .Lg2_ratio_done
	s_cmp_eq_u32 s12, 0
	v_mov_b32_e32 v2, 1.0
	s_cbranch_scc1 .LBB4_10
	v_lshl_add_u32 v2, v221, 2, s20
	v_lshl_add_u32 v3, v0, 2, s20
	ds_read_b32 v3, v3 offset:3072
	ds_read_b32 v2, v2 offset:6144
	s_waitcnt lgkmcnt(0)
	v_add_f32_e32 v2, v3, v2
.LBB4_10:
	v_lshl_add_u32 v221, v221, 2, s20
	ds_read2st64_b32 v[4:5], v221 offset0:16 offset1:20
	v_lshl_add_u32 v3, v0, 2, s20
	ds_read_b32 v3, v3 offset:7168
	ds_read_b32 v6, v221 offset:8192
	s_waitcnt lgkmcnt(1)
	v_add_f32_e32 v3, v4, v3
	v_div_scale_f32 v4, s[52:53], v3, v3, v2
	v_rcp_f32_e32 v7, v4
	s_waitcnt lgkmcnt(0)
	v_add_f32_e32 v5, v5, v6
	v_div_scale_f32 v6, vcc, v2, v3, v2
	v_fma_f32 v8, -v4, v7, 1.0
	v_fmac_f32_e32 v7, v8, v7
	v_mul_f32_e32 v8, v6, v7
	v_fma_f32 v9, -v4, v8, v6
	v_fmac_f32_e32 v8, v9, v7
	v_fma_f32 v4, -v4, v8, v6
	v_div_scale_f32 v6, s[52:53], v5, v5, v3
	v_rcp_f32_e32 v9, v6
	v_div_fmas_f32 v4, v4, v7, v8
	v_div_fixup_f32 v2, v4, v3, v2
	v_fma_f32 v4, -v6, v9, 1.0
	v_fmac_f32_e32 v9, v4, v9
	v_div_scale_f32 v4, vcc, v3, v5, v3
	v_mul_f32_e32 v7, v4, v9
	v_fma_f32 v8, -v6, v7, v4
	v_fmac_f32_e32 v7, v8, v9
	v_fma_f32 v4, -v6, v7, v4
	v_div_fmas_f32 v4, v4, v9, v7
	v_div_fixup_f32 v3, v4, v5, v3
	ds_write2st64_b32 v221, v2, v3 offset1:4
	ds_write_b32 v221, v5 offset:2048
.Lg2_ratio_done:
	s_or_b64 exec, exec, s[50:51]
	v_cmp_ne_u32_e32 vcc, 0, v132
	s_and_saveexec_b64 s[18:19], vcc
	s_cbranch_execz .LBB4_13
	s_barrier

.LBB4_20:
	s_or_b64 exec, exec, s[2:3]
	v_lshlrev_b32_e32 v1, 5, v136
	v_or3_b32 v133, v1, v135, s13
	v_lshlrev_b32_e32 v1, 7, v136
	v_lshlrev_b32_e32 v130, 2, v135
	v_add3_u32 v1, s20, v1, v130
	v_add_u32_e32 v137, 0x800, v1
	v_lshlrev_b32_e32 v131, 2, v134
	ds_read2_b32 v[134:135], v137 offset1:16
	s_ashr_i32 s13, s12, 31
	s_lshl_b64 s[0:1], s[12:13], 23
	v_and_b32_e32 v130, 16, v0
	s_add_u32 s0, s14, s0
	s_waitcnt lgkmcnt(0)
	v_mul_f32_e32 v134, 0x3d800000, v134
	v_pk_mul_f32 v[104:105], v[134:135], v[104:105] op_sel_hi:[0,1]
	v_pk_mul_f32 v[102:103], v[134:135], v[102:103] op_sel_hi:[0,1]
	v_pk_mul_f32 v[98:99], v[134:135], v[98:99] op_sel_hi:[0,1]
	v_cvt_pk_f16_f32 v102, v102, v103
	v_cvt_pk_f16_f32 v103, v104, v105
	v_cvt_pk_f16_f32 v104, v98, v99
	v_mul_f32_e32 v98, 0x3d800000, v135
	v_pk_mul_f32 v[72:73], v[98:99], v[72:73] op_sel_hi:[0,1]
	v_pk_mul_f32 v[70:71], v[98:99], v[70:71] op_sel_hi:[0,1]
	v_pk_mul_f32 v[66:67], v[98:99], v[66:67] op_sel_hi:[0,1]
	v_cvt_pk_f16_f32 v70, v70, v71
	v_cvt_pk_f16_f32 v71, v72, v73
	v_cvt_pk_f16_f32 v72, v66, v67
	ds_read2_b32 v[66:67], v137 offset0:128 offset1:144
	v_lshlrev_b32_e32 v0, 6, v0
	v_and_or_b32 v136, v131, 8, v130
	s_addc_u32 s1, s15, s1
	v_and_b32_e32 v0, 64, v0
	v_mov_b32_e32 v1, 0
	v_lshl_add_u64 v[130:131], s[0:1], 0, v[0:1]
	v_lshlrev_b32_e32 v0, 1, v136
	v_lshl_add_u64 v[130:131], v[130:131], 0, v[0:1]
	v_lshlrev_b32_e32 v0, 11, v133
	v_and_b32_e32 v0, 0x7b7000, v0
	s_waitcnt lgkmcnt(0)
	v_mul_f32_e32 v66, 0x3d800000, v66
	v_lshl_add_u64 v[130:131], v[130:131], 0, v[0:1]
	v_pk_mul_f32 v[100:101], v[134:135], v[100:101] op_sel_hi:[0,1]
	s_mov_b64 s[0:1], 0x8000
	v_pk_mul_f32 v[48:49], v[66:67], v[48:49] op_sel_hi:[0,1]
	v_pk_mul_f32 v[46:47], v[66:67], v[46:47] op_sel_hi:[0,1]
	v_pk_mul_f32 v[38:39], v[66:67], v[38:39] op_sel_hi:[0,1]
	v_pk_mul_f32 v[28:29], v[66:67], v[28:29] op_sel_hi:[0,1]
	v_pk_mul_f32 v[26:27], v[66:67], v[26:27] op_sel_hi:[0,1]
	v_lshlrev_b32_e32 v0, 8, v132
	v_cvt_pk_f16_f32 v105, v100, v101
	v_lshl_add_u64 v[100:101], v[130:131], 0, s[0:1]
	v_pk_mul_f32 v[68:69], v[98:99], v[68:69] op_sel_hi:[0,1]
	s_mov_b64 s[0:1], 0x40000
	v_cvt_pk_f16_f32 v46, v46, v47
	v_cvt_pk_f16_f32 v47, v48, v49
	v_cvt_pk_f16_f32 v48, v38, v39
	v_cvt_pk_f16_f32 v26, v26, v27
	v_cvt_pk_f16_f32 v27, v28, v29
	v_pk_mul_f32 v[38:39], v[66:67], v[44:45] op_sel_hi:[0,1]
	v_pk_mul_f32 v[28:29], v[66:67], v[42:43] op_sel_hi:[0,1]
	v_lshl_or_b32 v0, s21, 2, v0
	v_cvt_pk_f16_f32 v73, v68, v69
	v_lshl_add_u64 v[68:69], v[130:131], 0, s[0:1]
	v_pk_mul_f32 v[64:65], v[66:67], v[64:65] op_sel_hi:[0,1]
	v_pk_mul_f32 v[62:63], v[66:67], v[62:63] op_sel_hi:[0,1]
	v_pk_mul_f32 v[58:59], v[66:67], v[58:59] op_sel_hi:[0,1]
	v_cvt_pk_f16_f32 v28, v28, v29
	v_cvt_pk_f16_f32 v29, v38, v39
	v_cvt_pk_f16_f32 v62, v62, v63
	v_cvt_pk_f16_f32 v63, v64, v65
	v_cvt_pk_f16_f32 v64, v58, v59
	v_lshl_add_u64 v[58:59], v[68:69], 0, v[0:1]
	v_pk_mul_f32 v[40:41], v[66:67], v[40:41] op_sel_hi:[0,1]
	v_permlane16_swap_b32_e32 v26, v28
	v_permlane16_swap_b32_e32 v27, v29
	v_mul_f32_e32 v38, 0x3d800000, v67
	s_mov_b64 s[0:1], 0x48000
	v_pk_mul_f32 v[128:129], v[134:135], v[128:129] op_sel_hi:[0,1]
	v_pk_mul_f32 v[126:127], v[134:135], v[126:127] op_sel_hi:[0,1]
	v_pk_mul_f32 v[122:123], v[134:135], v[122:123] op_sel_hi:[0,1]
	v_pk_mul_f32 v[96:97], v[98:99], v[96:97] op_sel_hi:[0,1]
	v_pk_mul_f32 v[94:95], v[98:99], v[94:95] op_sel_hi:[0,1]
	v_pk_mul_f32 v[90:91], v[98:99], v[90:91] op_sel_hi:[0,1]
	v_pk_mul_f32 v[88:89], v[98:99], v[88:89] op_sel_hi:[0,1]
	v_pk_mul_f32 v[86:87], v[98:99], v[86:87] op_sel_hi:[0,1]
	v_pk_mul_f32 v[82:83], v[98:99], v[82:83] op_sel_hi:[0,1]
	v_cvt_pk_f16_f32 v49, v40, v41
	global_store_dwordx4 v[58:59], v[26:29], off offset:640
	v_lshl_add_u64 v[40:41], v[130:131], 0, s[0:1]
	v_cvt_pk_f16_f32 v126, v126, v127
	v_pk_mul_f32 v[28:29], v[38:39], v[36:37] op_sel_hi:[0,1]
	v_pk_mul_f32 v[26:27], v[38:39], v[34:35] op_sel_hi:[0,1]
	v_cvt_pk_f16_f32 v127, v128, v129
	v_cvt_pk_f16_f32 v128, v122, v123
	v_lshl_add_u64 v[122:123], v[130:131], 0, v[0:1]
	v_cvt_pk_f16_f32 v94, v94, v95
	v_cvt_pk_f16_f32 v95, v96, v97
	v_cvt_pk_f16_f32 v96, v90, v91
	v_lshl_add_u64 v[90:91], v[100:101], 0, v[0:1]
	v_cvt_pk_f16_f32 v86, v86, v87
	v_cvt_pk_f16_f32 v87, v88, v89
	v_cvt_pk_f16_f32 v88, v82, v83
	v_or_b32_e32 v82, 0x80, v0
	v_mov_b32_e32 v83, v1
	v_cvt_pk_f16_f32 v26, v26, v27
	v_cvt_pk_f16_f32 v27, v28, v29
	v_pk_mul_f32 v[28:29], v[38:39], v[30:31] op_sel_hi:[0,1]
	v_lshl_add_u64 v[30:31], v[40:41], 0, v[0:1]
	v_pk_mul_f32 v[0:1], v[38:39], v[24:25] op_sel_hi:[0,1]
	v_pk_mul_f32 v[22:23], v[38:39], v[22:23] op_sel_hi:[0,1]
	v_cvt_pk_f16_f32 v22, v22, v23
	v_cvt_pk_f16_f32 v23, v0, v1
	v_pk_mul_f32 v[0:1], v[38:39], v[20:21] op_sel_hi:[0,1]
	v_pk_mul_f32 v[18:19], v[38:39], v[18:19] op_sel_hi:[0,1]
	v_cvt_pk_f16_f32 v24, v18, v19
	v_cvt_pk_f16_f32 v25, v0, v1
	s_nop 0
	v_permlane16_swap_b32_e32 v22, v24
	v_permlane16_swap_b32_e32 v23, v25
	v_lshl_add_u64 v[0:1], v[40:41], 0, v[82:83]
	global_store_dwordx4 v[0:1], v[22:25], off
	v_pk_mul_f32 v[12:13], v[38:39], v[12:13] op_sel_hi:[0,1]
	v_pk_mul_f32 v[0:1], v[38:39], v[10:11] op_sel_hi:[0,1]
	v_pk_mul_f32 v[4:5], v[38:39], v[4:5] op_sel_hi:[0,1]
	v_pk_mul_f32 v[2:3], v[38:39], v[2:3] op_sel_hi:[0,1]
	v_cvt_pk_f16_f32 v0, v0, v1
	v_cvt_pk_f16_f32 v1, v12, v13
	v_cvt_pk_f16_f32 v2, v2, v3
	v_cvt_pk_f16_f32 v3, v4, v5
	s_nop 0
	v_permlane16_swap_b32_e32 v0, v2
	v_permlane16_swap_b32_e32 v1, v3
	global_store_dwordx4 v[30:31], v[0:3], off offset:512
	v_pk_mul_f32 v[124:125], v[134:135], v[124:125] op_sel_hi:[0,1]
	v_pk_mul_f32 v[120:121], v[134:135], v[120:121] op_sel_hi:[0,1]
	v_pk_mul_f32 v[2:3], v[38:39], v[16:17] op_sel_hi:[0,1]
	v_pk_mul_f32 v[0:1], v[38:39], v[14:15] op_sel_hi:[0,1]
	v_pk_mul_f32 v[118:119], v[134:135], v[118:119] op_sel_hi:[0,1]
	v_pk_mul_f32 v[116:117], v[134:135], v[116:117] op_sel_hi:[0,1]
	v_pk_mul_f32 v[114:115], v[134:135], v[114:115] op_sel_hi:[0,1]
	v_pk_mul_f32 v[112:113], v[134:135], v[112:113] op_sel_hi:[0,1]
	v_pk_mul_f32 v[110:111], v[134:135], v[110:111] op_sel_hi:[0,1]
	v_pk_mul_f32 v[108:109], v[134:135], v[108:109] op_sel_hi:[0,1]
	v_pk_mul_f32 v[106:107], v[134:135], v[106:107] op_sel_hi:[0,1]
	v_pk_mul_f32 v[92:93], v[98:99], v[92:93] op_sel_hi:[0,1]
	v_pk_mul_f32 v[84:85], v[98:99], v[84:85] op_sel_hi:[0,1]
	v_pk_mul_f32 v[80:81], v[98:99], v[80:81] op_sel_hi:[0,1]
	v_pk_mul_f32 v[78:79], v[98:99], v[78:79] op_sel_hi:[0,1]
	v_pk_mul_f32 v[76:77], v[98:99], v[76:77] op_sel_hi:[0,1]
	v_pk_mul_f32 v[74:75], v[98:99], v[74:75] op_sel_hi:[0,1]
	v_pk_mul_f32 v[60:61], v[66:67], v[60:61] op_sel_hi:[0,1]
	v_pk_mul_f32 v[56:57], v[66:67], v[56:57] op_sel_hi:[0,1]
	v_pk_mul_f32 v[54:55], v[66:67], v[54:55] op_sel_hi:[0,1]
	v_pk_mul_f32 v[52:53], v[66:67], v[52:53] op_sel_hi:[0,1]
	v_pk_mul_f32 v[50:51], v[66:67], v[50:51] op_sel_hi:[0,1]
	v_pk_mul_f32 v[32:33], v[38:39], v[32:33] op_sel_hi:[0,1]
	v_cvt_pk_f16_f32 v0, v0, v1
	v_cvt_pk_f16_f32 v1, v2, v3
	v_pk_mul_f32 v[4:5], v[38:39], v[8:9] op_sel_hi:[0,1]
	v_pk_mul_f32 v[2:3], v[38:39], v[6:7] op_sel_hi:[0,1]
	v_cvt_pk_f16_f32 v129, v124, v125
	v_cvt_pk_f16_f32 v118, v118, v119
	v_cvt_pk_f16_f32 v119, v120, v121
	v_cvt_pk_f16_f32 v120, v114, v115
	v_cvt_pk_f16_f32 v121, v116, v117
	v_cvt_pk_f16_f32 v110, v110, v111
	v_cvt_pk_f16_f32 v111, v112, v113
	v_cvt_pk_f16_f32 v112, v106, v107
	v_cvt_pk_f16_f32 v113, v108, v109
	v_cvt_pk_f16_f32 v97, v92, v93
	v_cvt_pk_f16_f32 v89, v84, v85
	v_cvt_pk_f16_f32 v78, v78, v79
	v_cvt_pk_f16_f32 v79, v80, v81
	v_cvt_pk_f16_f32 v80, v74, v75
	v_cvt_pk_f16_f32 v81, v76, v77
	v_cvt_pk_f16_f32 v65, v60, v61
	v_cvt_pk_f16_f32 v54, v54, v55
	v_cvt_pk_f16_f32 v55, v56, v57
	v_cvt_pk_f16_f32 v56, v50, v51
	v_cvt_pk_f16_f32 v57, v52, v53
	v_cvt_pk_f16_f32 v28, v28, v29
	v_cvt_pk_f16_f32 v29, v32, v33
	v_cvt_pk_f16_f32 v2, v2, v3
	v_cvt_pk_f16_f32 v3, v4, v5
	v_permlane16_swap_b32_e32 v126, v128
	v_permlane16_swap_b32_e32 v127, v129
	v_permlane16_swap_b32_e32 v118, v120
	v_permlane16_swap_b32_e32 v119, v121
	v_permlane16_swap_b32_e32 v110, v112
	v_permlane16_swap_b32_e32 v111, v113
	v_permlane16_swap_b32_e32 v102, v104
	v_permlane16_swap_b32_e32 v103, v105
	v_permlane16_swap_b32_e32 v94, v96
	v_permlane16_swap_b32_e32 v95, v97
	v_permlane16_swap_b32_e32 v86, v88
	v_permlane16_swap_b32_e32 v87, v89
	v_lshl_add_u64 v[84:85], v[100:101], 0, v[82:83]
	v_permlane16_swap_b32_e32 v78, v80
	v_permlane16_swap_b32_e32 v79, v81
	v_permlane16_swap_b32_e32 v70, v72
	v_permlane16_swap_b32_e32 v71, v73
	v_permlane16_swap_b32_e32 v62, v64
	v_permlane16_swap_b32_e32 v63, v65
	v_permlane16_swap_b32_e32 v54, v56
	v_permlane16_swap_b32_e32 v55, v57
	v_lshl_add_u64 v[50:51], v[68:69], 0, v[82:83]
	v_permlane16_swap_b32_e32 v46, v48
	v_permlane16_swap_b32_e32 v47, v49
	v_permlane16_swap_b32_e32 v26, v28
	v_permlane16_swap_b32_e32 v27, v29
	v_permlane16_swap_b32_e32 v0, v2
	v_permlane16_swap_b32_e32 v1, v3
	global_store_dwordx4 v[122:123], v[126:129], off
	global_store_dwordx4 v[122:123], v[118:121], off offset:128
	global_store_dwordx4 v[122:123], v[110:113], off offset:512
	global_store_dwordx4 v[122:123], v[102:105], off offset:640
	global_store_dwordx4 v[90:91], v[94:97], off
	global_store_dwordx4 v[84:85], v[86:89], off
	global_store_dwordx4 v[90:91], v[78:81], off offset:512
	global_store_dwordx4 v[90:91], v[70:73], off offset:640
	global_store_dwordx4 v[58:59], v[62:65], off
	global_store_dwordx4 v[50:51], v[54:57], off
	global_store_dwordx4 v[58:59], v[46:49], off offset:512
	global_store_dwordx4 v[30:31], v[26:29], off
	global_store_dwordx4 v[30:31], v[0:3], off offset:640
	s_endpgm
	.p2alignl 8, 3212836864

	.amdhsa_kernel _Z6gemm_kILi2EEvPKDF16_S1_iiiiPfPDF16_PKfS2_
		.amdhsa_group_segment_fixed_size 0
		.amdhsa_private_segment_fixed_size 0
		.amdhsa_kernarg_size 64
		.amdhsa_user_sgpr_count 2
		.amdhsa_user_sgpr_dispatch_ptr 0
		.amdhsa_user_sgpr_queue_ptr 0
		.amdhsa_user_sgpr_kernarg_segment_ptr 1
		.amdhsa_user_sgpr_dispatch_id 0
		.amdhsa_user_sgpr_kernarg_preload_length 0
		.amdhsa_user_sgpr_kernarg_preload_offset 0
		.amdhsa_user_sgpr_private_segment_size 0
		.amdhsa_uses_dynamic_stack 0
		.amdhsa_enable_private_segment 0
		.amdhsa_system_sgpr_workgroup_id_x 1
		.amdhsa_system_sgpr_workgroup_id_y 0
		.amdhsa_system_sgpr_workgroup_id_z 0
		.amdhsa_system_sgpr_workgroup_info 0
		.amdhsa_system_vgpr_workitem_id 0
		.amdhsa_next_free_vgpr 224
		.amdhsa_next_free_sgpr 54
		.amdhsa_accum_offset 224
		.amdhsa_reserve_vcc 1
		.amdhsa_float_round_mode_32 0
		.amdhsa_float_round_mode_16_64 0
		.amdhsa_float_denorm_mode_32 3
		.amdhsa_float_denorm_mode_16_64 3
		.amdhsa_dx10_clamp 1
		.amdhsa_ieee_mode 1
		.amdhsa_fp16_overflow 0
		.amdhsa_tg_split 0
		.amdhsa_exception_fp_ieee_invalid_op 0
		.amdhsa_exception_fp_denorm_src 0
		.amdhsa_exception_fp_ieee_div_zero 0
		.amdhsa_exception_fp_ieee_overflow 0
		.amdhsa_exception_fp_ieee_underflow 0
		.amdhsa_exception_fp_ieee_inexact 0
		.amdhsa_exception_int_div_zero 0
	.end_amdhsa_kernel

	.text
	.p2alignl 8, 3212836864
	.fill 256, 4, 3212836864

amdhsa.kernels:
  - .agpr_count:     0
    .args:
      - .actual_access:  read_only
        .address_space:  global
        .offset:         0
        .size:           8
        .value_kind:     global_buffer
      - .actual_access:  read_only
        .address_space:  global
        .offset:         8
        .size:           8
        .value_kind:     global_buffer
      - .actual_access:  read_only
        .address_space:  global
        .offset:         16
        .size:           8
        .value_kind:     global_buffer
      - .actual_access:  write_only
        .address_space:  global
        .offset:         24
        .size:           8
        .value_kind:     global_buffer
      - .actual_access:  write_only
        .address_space:  global
        .offset:         32
        .size:           8
        .value_kind:     global_buffer
      - .actual_access:  write_only
        .address_space:  global
        .offset:         40
        .size:           8
        .value_kind:     global_buffer
      - .actual_access:  write_only
        .address_space:  global
        .offset:         48
        .size:           8
        .value_kind:     global_buffer
      - .actual_access:  read_only
        .address_space:  global
        .offset:         56
        .size:           8
        .value_kind:     global_buffer
      - .actual_access:  read_only
        .address_space:  global
        .offset:         64
        .size:           8
        .value_kind:     global_buffer
      - .actual_access:  write_only
        .address_space:  global
        .offset:         72
        .size:           8
        .value_kind:     global_buffer
    .group_segment_fixed_size: 8448
    .kernarg_segment_align: 8
    .kernarg_segment_size: 80
    .language:       OpenCL C
    .language_version:
      - 2
      - 0
    .max_flat_workgroup_size: 256
    .name:           _Z6prep_kPKfS0_S0_PDF16_S1_S1_S1_S1_S0_Pf
    .private_segment_fixed_size: 0
    .sgpr_count:     20
    .sgpr_spill_count: 0
    .symbol:         _Z6prep_kPKfS0_S0_PDF16_S1_S1_S1_S1_S0_Pf.kd
    .uniform_work_group_size: 1
    .uses_dynamic_stack: false
    .vgpr_count:     34
    .vgpr_spill_count: 0
    .wavefront_size: 64
  - .agpr_count:     0
    .args:
      - .actual_access:  read_only
        .address_space:  global
        .offset:         0
        .size:           8
        .value_kind:     global_buffer
      - .actual_access:  write_only
        .address_space:  global
        .offset:         8
        .size:           8
        .value_kind:     global_buffer
      - .actual_access:  read_only
        .address_space:  global
        .offset:         16
        .size:           8
        .value_kind:     global_buffer
      - .actual_access:  write_only
        .address_space:  global
        .offset:         24
        .size:           8
        .value_kind:     global_buffer
      - .offset:         32
        .size:           4
        .value_kind:     hidden_block_count_x
      - .offset:         36
        .size:           4
        .value_kind:     hidden_block_count_y
      - .offset:         40
        .size:           4
        .value_kind:     hidden_block_count_z
      - .offset:         44
        .size:           2
        .value_kind:     hidden_group_size_x
      - .offset:         46
        .size:           2
        .value_kind:     hidden_group_size_y
      - .offset:         48
        .size:           2
        .value_kind:     hidden_group_size_z
      - .offset:         50
        .size:           2
        .value_kind:     hidden_remainder_x
      - .offset:         52
        .size:           2
        .value_kind:     hidden_remainder_y
      - .offset:         54
        .size:           2
        .value_kind:     hidden_remainder_z
      - .offset:         72
        .size:           8
        .value_kind:     hidden_global_offset_x
      - .offset:         80
        .size:           8
        .value_kind:     hidden_global_offset_y
      - .offset:         88
        .size:           8
        .value_kind:     hidden_global_offset_z
      - .offset:         96
        .size:           2
        .value_kind:     hidden_grid_dims
    .group_segment_fixed_size: 0
    .kernarg_segment_align: 8
    .kernarg_segment_size: 288
    .language:       OpenCL C
    .language_version:
      - 2
      - 0
    .max_flat_workgroup_size: 1024
    .name:           _Z6post_kPKfPfPKDF16_PDF16_
    .private_segment_fixed_size: 0
    .sgpr_count:     14
    .sgpr_spill_count: 0
    .symbol:         _Z6post_kPKfPfPKDF16_PDF16_.kd
    .uniform_work_group_size: 1
    .uses_dynamic_stack: false
    .vgpr_count:     49
    .vgpr_spill_count: 0
    .wavefront_size: 64
  - .agpr_count:     0
    .args:
      - .actual_access:  read_only
        .address_space:  global
        .offset:         0
        .size:           8
        .value_kind:     global_buffer
      - .actual_access:  read_only
        .address_space:  global
        .offset:         8
        .size:           8
        .value_kind:     global_buffer
      - .actual_access:  write_only
        .address_space:  global
        .offset:         16
        .size:           8
        .value_kind:     global_buffer
      - .offset:         24
        .size:           4
        .value_kind:     hidden_block_count_x
      - .offset:         28
        .size:           4
        .value_kind:     hidden_block_count_y
      - .offset:         32
        .size:           4
        .value_kind:     hidden_block_count_z
      - .offset:         36
        .size:           2
        .value_kind:     hidden_group_size_x
      - .offset:         38
        .size:           2
        .value_kind:     hidden_group_size_y
      - .offset:         40
        .size:           2
        .value_kind:     hidden_group_size_z
      - .offset:         42
        .size:           2
        .value_kind:     hidden_remainder_x
      - .offset:         44
        .size:           2
        .value_kind:     hidden_remainder_y
      - .offset:         46
        .size:           2
        .value_kind:     hidden_remainder_z
      - .offset:         64
        .size:           8
        .value_kind:     hidden_global_offset_x
      - .offset:         72
        .size:           8
        .value_kind:     hidden_global_offset_y
      - .offset:         80
        .size:           8
        .value_kind:     hidden_global_offset_z
      - .offset:         88
        .size:           2
        .value_kind:     hidden_grid_dims
    .group_segment_fixed_size: 0
    .kernarg_segment_align: 8
    .kernarg_segment_size: 280
    .language:       OpenCL C
    .language_version:
      - 2
      - 0
    .max_flat_workgroup_size: 1024
    .name:           _Z8reduce_kPKDF16_PKfPf
    .private_segment_fixed_size: 0
    .sgpr_count:     16
    .sgpr_spill_count: 0
    .symbol:         _Z8reduce_kPKDF16_PKfPf.kd
    .uniform_work_group_size: 1
    .uses_dynamic_stack: false
    .vgpr_count:     42
    .vgpr_spill_count: 0
    .wavefront_size: 64
  - .agpr_count:     0
    .args:
      - .actual_access:  read_only
        .address_space:  global
        .offset:         0
        .size:           8
        .value_kind:     global_buffer
      - .actual_access:  read_only
        .address_space:  global
        .offset:         8
        .size:           8
        .value_kind:     global_buffer
      - .actual_access:  write_only
        .address_space:  global
        .offset:         16
        .size:           8
        .value_kind:     global_buffer
      - .address_space:  global
        .offset:         24
        .size:           8
        .value_kind:     global_buffer
      - .actual_access:  write_only
        .address_space:  global
        .offset:         32
        .size:           8
        .value_kind:     global_buffer
      - .actual_access:  read_only
        .address_space:  global
        .offset:         40
        .size:           8
        .value_kind:     global_buffer
      - .actual_access:  write_only
        .address_space:  global
        .offset:         48
        .size:           8
        .value_kind:     global_buffer
    .group_segment_fixed_size: 0
    .kernarg_segment_align: 8
    .kernarg_segment_size: 56
    .language:       OpenCL C
    .language_version:
      - 2
      - 0
    .max_flat_workgroup_size: 512
    .name:           _Z7gemm1_kPKDF16_S0_PDF16_PKfPfS0_S1_
    .private_segment_fixed_size: 0
    .sgpr_count:     62
    .sgpr_spill_count: 0
    .symbol:         _Z7gemm1_kPKDF16_S0_PDF16_PKfPfS0_S1_.kd
    .uniform_work_group_size: 1
    .uses_dynamic_stack: false
    .vgpr_count:     228
    .vgpr_spill_count: 0
    .wavefront_size: 64
  - .agpr_count:     0
    .args:
      - .actual_access:  read_only
        .address_space:  global
        .offset:         0
        .size:           8
        .value_kind:     global_buffer
      - .actual_access:  read_only
        .address_space:  global
        .offset:         8
        .size:           8
        .value_kind:     global_buffer
      - .offset:         16
        .size:           4
        .value_kind:     by_value
      - .offset:         20
        .size:           4
        .value_kind:     by_value
      - .offset:         24
        .size:           4
        .value_kind:     by_value
      - .offset:         28
        .size:           4
        .value_kind:     by_value
      - .actual_access:  read_only
        .address_space:  global
        .offset:         32
        .size:           8
        .value_kind:     global_buffer
      - .actual_access:  write_only
        .address_space:  global
        .offset:         40
        .size:           8
        .value_kind:     global_buffer
      - .actual_access:  read_only
        .address_space:  global
        .offset:         48
        .size:           8
        .value_kind:     global_buffer
      - .actual_access:  read_only
        .address_space:  global
        .offset:         56
        .size:           8
        .value_kind:     global_buffer
    .group_segment_fixed_size: 0
    .kernarg_segment_align: 8
    .kernarg_segment_size: 64
    .language:       OpenCL C
    .language_version:
      - 2
      - 0
    .max_flat_workgroup_size: 512
    .name:           _Z6gemm_kILi2EEvPKDF16_S1_iiiiPfPDF16_PKfS2_
    .private_segment_fixed_size: 0
    .sgpr_count:     60
    .sgpr_spill_count: 0
    .symbol:         _Z6gemm_kILi2EEvPKDF16_S1_iiiiPfPDF16_PKfS2_.kd
    .uniform_work_group_size: 1
    .uses_dynamic_stack: false
    .vgpr_count:     224
    .vgpr_spill_count: 0
    .wavefront_size: 64
  - .agpr_count:     0
    .args:
      - .actual_access:  read_only
        .address_space:  global
        .offset:         0
        .size:           8
        .value_kind:     global_buffer
      - .actual_access:  read_only
        .address_space:  global
        .offset:         8
        .size:           8
        .value_kind:     global_buffer
      - .offset:         16
        .size:           4
        .value_kind:     by_value
      - .offset:         20
        .size:           4
        .value_kind:     by_value
      - .offset:         24
        .size:           4
        .value_kind:     by_value
      - .offset:         28
        .size:           4
        .value_kind:     by_value
      - .actual_access:  read_only
        .address_space:  global
        .offset:         32
        .size:           8
        .value_kind:     global_buffer
      - .actual_access:  write_only
        .address_space:  global
        .offset:         40
        .size:           8
        .value_kind:     global_buffer
      - .actual_access:  read_only
        .address_space:  global
        .offset:         48
        .size:           8
        .value_kind:     global_buffer
      - .actual_access:  read_only
        .address_space:  global
        .offset:         56
        .size:           8
        .value_kind:     global_buffer
    .group_segment_fixed_size: 0
    .kernarg_segment_align: 8
    .kernarg_segment_size: 64
    .language:       OpenCL C
    .language_version:
      - 2
      - 0
    .max_flat_workgroup_size: 512
    .name:           _Z6gemm_kILi3EEvPKDF16_S1_iiiiPfPDF16_PKfS2_
    .private_segment_fixed_size: 0
    .sgpr_count:     51
    .sgpr_spill_count: 0
    .symbol:         _Z6gemm_kILi3EEvPKDF16_S1_iiiiPfPDF16_PKfS2_.kd
    .uniform_work_group_size: 1
    .uses_dynamic_stack: false
    .vgpr_count:     220
    .vgpr_spill_count: 0
    .wavefront_size: 64
